# speedup vs baseline: 1.0481x; 1.0481x over previous
_Z16sum_layer_kernelPKfS0_Pf:
	s_load_dwordx4 s[4:7], s[0:1], 0x0
	s_load_dwordx2 s[8:9], s[0:1], 0x10
	v_and_b32_e32 v40, 31, v0
	v_bfe_u32 v41, v0, 5, 1
	v_lshrrev_b32_e32 v42, 6, v0
	v_and_b32_e32 v43, 7, v0
	v_bfe_u32 v44, v0, 3, 3
	v_and_b32_e32 v45, 63, v0
	s_lshl_b32 s3, s2, 12
	s_lshl_b32 s19, s2, 7
	v_lshlrev_b32_e32 v1, 11, v41
	v_lshl_or_b32 v1, v40, 2, v1
	v_lshlrev_b32_e32 v46, 4, v43
	v_lshl_add_u32 v35, v44, 16, v46
	v_lshl_add_u32 v35, v42, 21, v35
	v_add_u32_e32 v35, s19, v35
	v_lshlrev_b32_e32 v36, 2, v40
	v_lshl_add_u32 v36, v41, 18, v36
	v_lshl_add_u32 v36, v42, 21, v36
	v_add_u32_e32 v36, s19, v36
	v_mul_u32_u24_e32 v37, 0x1200, v42
	v_mul_u32_u24_e32 v38, 0x90, v44
	v_add3_u32 v38, v37, v38, v46
	v_mul_u32_u24_e32 v39, 0x90, v40
	v_lshlrev_b32_e32 v47, 6, v41
	v_add3_u32 v39, v37, v39, v47
	v_lshrrev_b32_e32 v46, 1, v44
	v_xor_b32_e32 v46, v43, v46
	v_lshlrev_b32_e32 v46, 4, v46
	v_lshl_add_u32 v35, v44, 16, v46
	v_lshl_add_u32 v35, v42, 21, v35
	v_add_u32_e32 v35, s19, v35
	v_xor_b32_e32 v86, 64, v35
	v_readfirstlane_b32 s23, v42
	v_bfe_u32 v47, v40, 1, 3
	v_lshlrev_b32_e32 v39, 2, v41
	v_xor_b32_e32 v39, v39, v47
	s_lshl_b32 s23, s23, 12
	v_lshlrev_b32_e32 v39, 4, v39
	v_lshl_add_u32 v39, v40, 7, v39
	v_lshl_add_u32 v39, v42, 12, v39
	s_mov_b32 m0, s23
	v_xor_b32_e32 v81, 16, v39
	v_xor_b32_e32 v82, 32, v39
	v_xor_b32_e32 v83, 48, v39
	v_cmp_gt_u32_e32 vcc, 32, v45
	v_mov_b32_e32 v34, 0xc1600000
	v_mov_b32_e32 v84, 0x3fb8aa3b
	v_mov_b32_e32 v85, 0x3f317218
	s_mov_b32 s16, 0x3fb8aa3b
	s_mov_b32 s17, 0x3f317218
	s_mov_b32 s20, 0x7fc00
	s_mov_b32 s21, 0xff800
	s_mov_b32 s22, 0x17f400
	s_lshl_b32 s24, 1, 16
	s_lshl_b32 s25, 2, 16
	s_lshl_b32 s26, 3, 16
	s_lshl_b32 s27, 8, 16
	s_lshl_b32 s28, 9, 16
	s_lshl_b32 s29, 10, 16
	s_lshl_b32 s30, 11, 16
	s_lshl_b32 s31, 16, 16
	s_lshl_b32 s32, 17, 16
	s_lshl_b32 s33, 18, 16
	s_lshl_b32 s34, 19, 16
	s_lshl_b32 s35, 24, 16
	s_lshl_b32 s36, 25, 16
	s_lshl_b32 s37, 26, 16
	s_lshl_b32 s38, 27, 16
	s_mov_b32 s14, 0x200000
	s_mov_b32 s15, 0x20000
	s_waitcnt lgkmcnt(0)
	s_mov_b32 s12, s6
	s_and_b32 s13, s7, 0xffff
	s_and_b32 s5, s5, 0xffff
	s_mov_b32 s6, 0x800000
	s_mov_b32 s7, s15
	s_and_b32 s9, s9, 0xffff
	s_mov_b32 s10, s6
	s_mov_b32 s11, s15
	buffer_load_dword v18, v1, s[12:15], s3 offen nt
	buffer_load_dword v19, v1, s[12:15], s3 offen offset:128 nt
	buffer_load_dword v20, v1, s[12:15], s3 offen offset:256 nt
	buffer_load_dword v21, v1, s[12:15], s3 offen offset:384 nt
	buffer_load_dword v22, v1, s[12:15], s3 offen offset:512 nt
	buffer_load_dword v23, v1, s[12:15], s3 offen offset:640 nt
	buffer_load_dword v24, v1, s[12:15], s3 offen offset:768 nt
	buffer_load_dword v25, v1, s[12:15], s3 offen offset:896 nt
	buffer_load_dword v26, v1, s[12:15], s3 offen offset:1024 nt
	buffer_load_dword v27, v1, s[12:15], s3 offen offset:1152 nt
	buffer_load_dword v28, v1, s[12:15], s3 offen offset:1280 nt
	buffer_load_dword v29, v1, s[12:15], s3 offen offset:1408 nt
	buffer_load_dword v30, v1, s[12:15], s3 offen offset:1536 nt
	buffer_load_dword v31, v1, s[12:15], s3 offen offset:1664 nt
	buffer_load_dword v32, v1, s[12:15], s3 offen offset:1792 nt
	buffer_load_dword v33, v1, s[12:15], s3 offen offset:1920 nt
	buffer_load_dwordx4 v35, s[4:7], 0 offen nt lds
	buffer_load_dwordx4 v86, s[4:7], s20 offen offset:1024 nt lds
	buffer_load_dwordx4 v35, s[4:7], s21 offen offset:2048 nt lds
	buffer_load_dwordx4 v86, s[4:7], s22 offen offset:3072 nt lds
	s_waitcnt vmcnt(4)
	v_max3_f32 v48, v18, v19, v20
	v_max3_f32 v50, v21, v22, v23
	v_max3_f32 v48, v48, v24, v25
	v_max3_f32 v50, v50, v26, v27
	v_max3_f32 v48, v48, v28, v29
	v_max3_f32 v50, v50, v30, v31
	v_max3_f32 v48, v48, v32, v33
	v_max_f32_e32 v48, v48, v50
	v_mov_b32_e32 v50, v48
	s_nop 1
	v_permlane32_swap_b32_e32 v48, v50
	v_max_f32_e32 v48, v48, v50
	v_fmamk_f32 v48, v48, 0x3fb8aa3b, v34
	v_pk_fma_f32 v[18:19], v[18:19], v[84:85], v[48:49] op_sel_hi:[1,0,0] neg_lo:[0,0,1] neg_hi:[0,0,1]
	v_exp_f32_e32 v18, v18
	v_exp_f32_e32 v19, v19
	v_pk_fma_f32 v[20:21], v[20:21], v[84:85], v[48:49] op_sel_hi:[1,0,0] neg_lo:[0,0,1] neg_hi:[0,0,1]
	v_exp_f32_e32 v20, v20
	v_exp_f32_e32 v21, v21
	v_pk_fma_f32 v[22:23], v[22:23], v[84:85], v[48:49] op_sel_hi:[1,0,0] neg_lo:[0,0,1] neg_hi:[0,0,1]
	v_exp_f32_e32 v22, v22
	v_exp_f32_e32 v23, v23
	v_pk_fma_f32 v[24:25], v[24:25], v[84:85], v[48:49] op_sel_hi:[1,0,0] neg_lo:[0,0,1] neg_hi:[0,0,1]
	v_exp_f32_e32 v24, v24
	v_exp_f32_e32 v25, v25
	v_pk_fma_f32 v[26:27], v[26:27], v[84:85], v[48:49] op_sel_hi:[1,0,0] neg_lo:[0,0,1] neg_hi:[0,0,1]
	v_exp_f32_e32 v26, v26
	v_exp_f32_e32 v27, v27
	v_pk_fma_f32 v[28:29], v[28:29], v[84:85], v[48:49] op_sel_hi:[1,0,0] neg_lo:[0,0,1] neg_hi:[0,0,1]
	v_exp_f32_e32 v28, v28
	v_exp_f32_e32 v29, v29
	v_pk_fma_f32 v[30:31], v[30:31], v[84:85], v[48:49] op_sel_hi:[1,0,0] neg_lo:[0,0,1] neg_hi:[0,0,1]
	v_exp_f32_e32 v30, v30
	v_exp_f32_e32 v31, v31
	v_pk_fma_f32 v[32:33], v[32:33], v[84:85], v[48:49] op_sel_hi:[1,0,0] neg_lo:[0,0,1] neg_hi:[0,0,1]
	v_exp_f32_e32 v32, v32
	v_exp_f32_e32 v33, v33
	v_pk_add_f32 v[56:57], v[18:19], v[20:21]
	v_pk_add_f32 v[58:59], v[22:23], v[24:25]
	v_pk_add_f32 v[60:61], v[26:27], v[28:29]
	v_pk_add_f32 v[62:63], v[30:31], v[32:33]
	v_pk_add_f32 v[56:57], v[56:57], v[58:59]
	v_pk_add_f32 v[60:61], v[60:61], v[62:63]
	v_pk_add_f32 v[56:57], v[56:57], v[60:61]
	v_add_f32_e32 v50, v56, v57
	v_mov_b32_e32 v51, v50
	s_nop 1
	v_permlane32_swap_b32_e32 v50, v51
	v_add_f32_e32 v50, v50, v51
	v_log_f32_e32 v50, v50
	v_cvt_pk_f16_f32 v40, v18, v19
	v_cvt_pk_f16_f32 v41, v20, v21
	v_cvt_pk_f16_f32 v42, v22, v23
	v_cvt_pk_f16_f32 v43, v24, v25
	v_cvt_pk_f16_f32 v44, v26, v27
	v_cvt_pk_f16_f32 v45, v28, v29
	v_cvt_pk_f16_f32 v46, v30, v31
	v_cvt_pk_f16_f32 v47, v32, v33
	v_add_f32_e32 v50, 0x41600000, v50
	v_mul_f32_e32 v50, 0xbf317218, v50
	v_cndmask_b32_e64 v51, v50, 1.0, vcc
	s_waitcnt vmcnt(0)
	ds_read_b128 v[2:5], v39
	ds_read_b128 v[6:9], v81
	ds_read_b128 v[10:13], v82
	ds_read_b128 v[14:17], v83
	s_waitcnt lgkmcnt(2)
	v_max3_f32 v52, v2, v3, v4
	v_max3_f32 v53, v5, v6, v7
	v_max_f32_e32 v52, v52, v8
	v_max_f32_e32 v53, v53, v9
	s_waitcnt lgkmcnt(0)
	v_max3_f32 v52, v52, v10, v11
	v_max3_f32 v53, v53, v12, v13
	v_max3_f32 v52, v52, v14, v15
	v_max3_f32 v53, v53, v16, v17
	v_max_f32_e32 v52, v52, v53
	v_mov_b32_e32 v53, v52
	s_nop 1
	v_permlane32_swap_b32_e32 v52, v53
	v_max_f32_e32 v52, v52, v53
	v_cndmask_b32_e32 v54, 1.0, v52, vcc
	v_fmamk_f32 v48, v52, 0x3fb8aa3b, v34
	v_pk_fma_f32 v[2:3], v[2:3], v[84:85], v[48:49] op_sel_hi:[1,0,0] neg_lo:[0,0,1] neg_hi:[0,0,1]
	v_mfma_f32_32x32x2_f32 v[64:79], v54, v51, 0
	v_exp_f32_e32 v2, v2
	v_exp_f32_e32 v3, v3
	v_pk_fma_f32 v[4:5], v[4:5], v[84:85], v[48:49] op_sel_hi:[1,0,0] neg_lo:[0,0,1] neg_hi:[0,0,1]
	v_exp_f32_e32 v4, v4
	v_exp_f32_e32 v5, v5
	v_pk_fma_f32 v[6:7], v[6:7], v[84:85], v[48:49] op_sel_hi:[1,0,0] neg_lo:[0,0,1] neg_hi:[0,0,1]
	v_exp_f32_e32 v6, v6
	v_exp_f32_e32 v7, v7
	v_pk_fma_f32 v[8:9], v[8:9], v[84:85], v[48:49] op_sel_hi:[1,0,0] neg_lo:[0,0,1] neg_hi:[0,0,1]
	v_exp_f32_e32 v8, v8
	v_exp_f32_e32 v9, v9
	v_pk_fma_f32 v[10:11], v[10:11], v[84:85], v[48:49] op_sel_hi:[1,0,0] neg_lo:[0,0,1] neg_hi:[0,0,1]
	v_exp_f32_e32 v10, v10
	v_cvt_pk_f16_f32 v56, v2, v3
	v_cvt_pk_f16_f32 v57, v4, v5
	v_cvt_pk_f16_f32 v58, v6, v7
	v_cvt_pk_f16_f32 v59, v8, v9
	v_exp_f32_e32 v11, v11
	v_pk_fma_f32 v[12:13], v[12:13], v[84:85], v[48:49] op_sel_hi:[1,0,0] neg_lo:[0,0,1] neg_hi:[0,0,1]
	v_exp_f32_e32 v12, v12
	v_mfma_f32_32x32x16_f16 v[18:33], v[56:59], v[40:43], 0
	v_exp_f32_e32 v13, v13
	v_pk_fma_f32 v[14:15], v[14:15], v[84:85], v[48:49] op_sel_hi:[1,0,0] neg_lo:[0,0,1] neg_hi:[0,0,1]
	v_exp_f32_e32 v14, v14
	v_exp_f32_e32 v15, v15
	v_pk_fma_f32 v[16:17], v[16:17], v[84:85], v[48:49] op_sel_hi:[1,0,0] neg_lo:[0,0,1] neg_hi:[0,0,1]
	v_exp_f32_e32 v16, v16
	v_exp_f32_e32 v17, v17
	v_cvt_pk_f16_f32 v60, v10, v11
	v_cvt_pk_f16_f32 v61, v12, v13
	v_cvt_pk_f16_f32 v62, v14, v15
	v_cvt_pk_f16_f32 v63, v16, v17
	s_nop 1
	v_mfma_f32_32x32x16_f16 v[18:33], v[60:63], v[44:47], v[18:33]
	s_nop 11
	v_log_f32_e32 v18, v18
	v_log_f32_e32 v19, v19
	v_log_f32_e32 v20, v20
	v_log_f32_e32 v21, v21
	v_log_f32_e32 v22, v22
	v_log_f32_e32 v23, v23
	v_pk_fma_f32 v[64:65], v[18:19], v[84:85], v[64:65] op_sel:[0,1,0] op_sel_hi:[1,1,1]
	buffer_store_dword v64, v36, s[8:11], 0 offen
	buffer_store_dword v65, v36, s[8:11], s24 offen
	v_log_f32_e32 v24, v24
	v_log_f32_e32 v25, v25
	v_pk_fma_f32 v[66:67], v[20:21], v[84:85], v[66:67] op_sel:[0,1,0] op_sel_hi:[1,1,1]
	buffer_store_dword v66, v36, s[8:11], s25 offen
	buffer_store_dword v67, v36, s[8:11], s26 offen
	v_log_f32_e32 v26, v26
	v_log_f32_e32 v27, v27
	v_pk_fma_f32 v[68:69], v[22:23], v[84:85], v[68:69] op_sel:[0,1,0] op_sel_hi:[1,1,1]
	buffer_store_dword v68, v36, s[8:11], s27 offen
	buffer_store_dword v69, v36, s[8:11], s28 offen
	v_log_f32_e32 v28, v28
	v_log_f32_e32 v29, v29
	v_pk_fma_f32 v[70:71], v[24:25], v[84:85], v[70:71] op_sel:[0,1,0] op_sel_hi:[1,1,1]
	buffer_store_dword v70, v36, s[8:11], s29 offen
	buffer_store_dword v71, v36, s[8:11], s30 offen
	v_log_f32_e32 v30, v30
	v_log_f32_e32 v31, v31
	v_pk_fma_f32 v[72:73], v[26:27], v[84:85], v[72:73] op_sel:[0,1,0] op_sel_hi:[1,1,1]
	buffer_store_dword v72, v36, s[8:11], s31 offen
	buffer_store_dword v73, v36, s[8:11], s32 offen
	v_log_f32_e32 v32, v32
	v_log_f32_e32 v33, v33
	v_pk_fma_f32 v[74:75], v[28:29], v[84:85], v[74:75] op_sel:[0,1,0] op_sel_hi:[1,1,1]
	buffer_store_dword v74, v36, s[8:11], s33 offen
	buffer_store_dword v75, v36, s[8:11], s34 offen
	v_pk_fma_f32 v[76:77], v[30:31], v[84:85], v[76:77] op_sel:[0,1,0] op_sel_hi:[1,1,1]
	buffer_store_dword v76, v36, s[8:11], s35 offen
	buffer_store_dword v77, v36, s[8:11], s36 offen
	v_pk_fma_f32 v[78:79], v[32:33], v[84:85], v[78:79] op_sel:[0,1,0] op_sel_hi:[1,1,1]
	buffer_store_dword v78, v36, s[8:11], s37 offen
	buffer_store_dword v79, v36, s[8:11], s38 offen
	s_endpgm
